# baseline (speedup 1.0000x reference)
.LBB1_36:
	s_or_b64 exec, exec, s[2:3]
	s_waitcnt vmcnt(0)
	v_add_f32_e32 v103, 0, v103
	v_add_f32_e32 v103, v103, v104
	v_add_f32_e32 v103, v103, v105
	v_add_f32_e32 v103, v103, v106
	v_add_f32_e32 v103, v103, v107
	v_add_f32_e32 v103, v103, v108
	v_add_f32_e32 v103, v103, v109
	v_add_f32_e32 v103, v103, v110
	v_add_f32_e32 v103, v103, v111
	v_add_f32_e32 v103, v103, v112
	v_add_f32_e32 v103, v103, v113
	v_add_f32_e32 v103, v103, v114
	v_add_f32_e32 v103, v103, v115
	v_add_f32_e32 v103, v103, v116
	v_add_f32_e32 v103, v103, v117
	v_add_f32_e32 v103, v103, v118
	v_add_f32_e32 v103, v103, v119
	v_add_f32_e32 v103, v103, v120
	v_add_f32_e32 v103, v103, v121
	v_add_f32_e32 v103, v103, v122
	s_mov_b32 s14, 0xf800000
	s_mov_b32 s11, 0x41e6d4ca
	v_cmp_gt_f32_e32 vcc, s14, v103
	v_mul_f32_e32 v104, 0x4f800000, v103
	s_nop 0
	v_cndmask_b32_e32 v104, v103, v104, vcc
	v_sqrt_f32_e32 v103, v104
	s_nop 0
	v_add_u32_e32 v105, -1, v103
	v_fma_f32 v108, -v105, v103, v104
	v_cmp_ge_f32_e64 s[2:3], 0, v108
	v_add_u32_e32 v108, 1, v103
	s_nop 0
	v_cndmask_b32_e64 v105, v103, v105, s[2:3]
	v_fma_f32 v103, -v108, v103, v104
	v_cmp_lt_f32_e64 s[2:3], 0, v103
	s_nop 1
	v_cndmask_b32_e64 v103, v105, v108, s[2:3]
	v_mul_f32_e32 v105, 0x37800000, v103
	v_cndmask_b32_e32 v105, v103, v105, vcc
	v_mov_b32_e32 v103, 0x260
	v_cmp_class_f32_e32 vcc, v104, v103
	s_nop 1
	v_cndmask_b32_e32 v104, v105, v104, vcc
	v_add_f32_e32 v104, 0x322bcc77, v104
	v_div_scale_f32 v108, s[2:3], v104, v104, s11
	v_rcp_f32_e32 v105, v108
	s_nop 0
	v_fma_f32 v109, -v108, v105, 1.0
	v_fmac_f32_e32 v105, v109, v105
	v_div_scale_f32 v107, vcc, s11, v104, s11
	v_mul_f32_e32 v106, v107, v105
	v_fma_f32 v111, -v108, v106, v107
	v_fmac_f32_e32 v106, v111, v105
	v_fma_f32 v107, -v108, v106, v107
	s_nop 0
	v_div_fmas_f32 v109, v107, v105, v106
	v_div_fixup_f32 v109, v109, v104, s11
	v_lshlrev_b32_e32 v110, 2, v101
	ds_bpermute_b32 v108, v110, v109
	ds_bpermute_b32 v111, v110, v109 offset:64
	ds_bpermute_b32 v112, v110, v109 offset:128
	ds_bpermute_b32 v113, v110, v109 offset:192
	s_mul_i32 s2, s23, 0x1f80
	s_add_i32 s6, s8, s2
	s_movk_i32 s2, 0x88
	v_and_b32_e32 v66, 0x70, v100
	v_add_u32_e32 v71, s10, v66
	v_lshrrev_b32_e32 v67, 4, v100
	v_lshlrev_b32_e32 v67, 3, v67
	v_add_u32_e32 v72, s6, v67
	s_mov_b32 s34, 0x3d0df4e0
	v_mad_u32_u24 v120, v101, s2, v72
	ds_read_b128 v[114:117], v71 offset:8832
	s_waitcnt lgkmcnt(0)
	v_mul_f32_e32 v118, v114, v108
	v_mul_f32_e32 v119, v115, v108
	v_mul_f32_e32 v121, v116, v108
	v_mul_f32_e32 v122, v117, v108
	v_fmaak_f32 v60, v60, v118, 0xc1e6d4ca
	v_fmaak_f32 v61, v61, v119, 0xc1e6d4ca
	v_fmaak_f32 v62, v62, v121, 0xc1e6d4ca
	v_fmaak_f32 v63, v63, v122, 0xc1e6d4ca
	v_exp_f32_e32 v64, v60
	v_mul_f32_e32 v118, v114, v111
	v_mul_f32_e32 v119, v115, v111
	v_fma_f32 v60, v60, s34, 1.0
	v_exp_f32_e32 v65, v61
	v_mul_f32_e32 v121, v116, v111
	v_mul_f32_e32 v122, v117, v111
	v_fma_f32 v61, v61, s34, 1.0
	v_exp_f32_e32 v66, v62
	v_fmaak_f32 v56, v56, v118, 0xc1e6d4ca
	v_fmaak_f32 v57, v57, v119, 0xc1e6d4ca
	v_fma_f32 v62, v62, s34, 1.0
	v_exp_f32_e32 v67, v63
	v_fmaak_f32 v58, v58, v121, 0xc1e6d4ca
	v_fmaak_f32 v59, v59, v122, 0xc1e6d4ca
	v_fma_f32 v63, v63, s34, 1.0
	v_mul_f32_e32 v60, v64, v60
	v_mul_f32_e32 v61, v65, v61
	v_cvt_pk_bf16_f32 v68, v64, v65
	v_mul_f32_e32 v62, v66, v62
	v_mul_f32_e32 v63, v67, v63
	v_cvt_pk_bf16_f32 v69, v66, v67
	ds_write_b64 v120, v[68:69] offset:10240
	v_cvt_pk_bf16_f32 v72, v60, v61
	v_cvt_pk_bf16_f32 v73, v62, v63
	v_exp_f32_e32 v64, v56
	v_mul_f32_e32 v118, v114, v112
	v_mul_f32_e32 v119, v115, v112
	v_fma_f32 v56, v56, s34, 1.0
	v_exp_f32_e32 v65, v57
	v_mul_f32_e32 v121, v116, v112
	v_mul_f32_e32 v122, v117, v112
	v_fma_f32 v57, v57, s34, 1.0
	v_exp_f32_e32 v66, v58
	v_fmaak_f32 v52, v52, v118, 0xc1e6d4ca
	v_fmaak_f32 v53, v53, v119, 0xc1e6d4ca
	v_fma_f32 v58, v58, s34, 1.0
	v_exp_f32_e32 v67, v59
	v_fmaak_f32 v54, v54, v121, 0xc1e6d4ca
	v_fmaak_f32 v55, v55, v122, 0xc1e6d4ca
	v_fma_f32 v59, v59, s34, 1.0
	v_mul_f32_e32 v56, v64, v56
	v_mul_f32_e32 v57, v65, v57
	v_cvt_pk_bf16_f32 v68, v64, v65
	v_mul_f32_e32 v58, v66, v58
	v_mul_f32_e32 v59, v67, v59
	v_cvt_pk_bf16_f32 v69, v66, v67
	ds_write_b64 v120, v[68:69] offset:12416
	v_cvt_pk_bf16_f32 v74, v56, v57
	v_cvt_pk_bf16_f32 v75, v58, v59
	v_exp_f32_e32 v64, v52
	v_mul_f32_e32 v118, v114, v113
	v_mul_f32_e32 v119, v115, v113
	v_fma_f32 v52, v52, s34, 1.0
	v_exp_f32_e32 v65, v53
	v_mul_f32_e32 v121, v116, v113
	v_mul_f32_e32 v122, v117, v113
	v_fma_f32 v53, v53, s34, 1.0
	ds_read_b128 v[114:117], v71 offset:8896
	v_exp_f32_e32 v66, v54
	v_fmaak_f32 v48, v48, v118, 0xc1e6d4ca
	v_fmaak_f32 v49, v49, v119, 0xc1e6d4ca
	v_fma_f32 v54, v54, s34, 1.0
	v_exp_f32_e32 v67, v55
	v_fmaak_f32 v50, v50, v121, 0xc1e6d4ca
	v_fmaak_f32 v51, v51, v122, 0xc1e6d4ca
	v_fma_f32 v55, v55, s34, 1.0
	v_mul_f32_e32 v52, v64, v52
	v_mul_f32_e32 v53, v65, v53
	v_cvt_pk_bf16_f32 v68, v64, v65
	v_mul_f32_e32 v54, v66, v54
	v_mul_f32_e32 v55, v67, v55
	v_cvt_pk_bf16_f32 v69, v66, v67
	ds_write_b64 v120, v[68:69] offset:14592
	v_cvt_pk_bf16_f32 v76, v52, v53
	v_cvt_pk_bf16_f32 v77, v54, v55
	s_waitcnt lgkmcnt(0)
	v_exp_f32_e32 v64, v48
	v_mul_f32_e32 v118, v114, v108
	v_mul_f32_e32 v119, v115, v108
	v_fma_f32 v48, v48, s34, 1.0
	v_exp_f32_e32 v65, v49
	v_mul_f32_e32 v121, v116, v108
	v_mul_f32_e32 v122, v117, v108
	v_fma_f32 v49, v49, s34, 1.0
	v_exp_f32_e32 v66, v50
	v_fmaak_f32 v44, v44, v118, 0xc1e6d4ca
	v_fmaak_f32 v45, v45, v119, 0xc1e6d4ca
	v_fma_f32 v50, v50, s34, 1.0
	v_exp_f32_e32 v67, v51
	v_fmaak_f32 v46, v46, v121, 0xc1e6d4ca
	v_fmaak_f32 v47, v47, v122, 0xc1e6d4ca
	v_fma_f32 v51, v51, s34, 1.0
	v_mul_f32_e32 v48, v64, v48
	v_mul_f32_e32 v49, v65, v49
	v_cvt_pk_bf16_f32 v68, v64, v65
	v_mul_f32_e32 v50, v66, v50
	v_mul_f32_e32 v51, v67, v51
	v_cvt_pk_bf16_f32 v69, v66, v67
	ds_write_b64 v120, v[68:69] offset:16768
	v_cvt_pk_bf16_f32 v78, v48, v49
	v_cvt_pk_bf16_f32 v79, v50, v51
	v_exp_f32_e32 v64, v44
	v_mul_f32_e32 v118, v114, v111
	v_mul_f32_e32 v119, v115, v111
	v_fma_f32 v44, v44, s34, 1.0
	v_exp_f32_e32 v65, v45
	v_mul_f32_e32 v121, v116, v111
	v_mul_f32_e32 v122, v117, v111
	v_fma_f32 v45, v45, s34, 1.0
	v_exp_f32_e32 v66, v46
	v_fmaak_f32 v40, v40, v118, 0xc1e6d4ca
	v_fmaak_f32 v41, v41, v119, 0xc1e6d4ca
	v_fma_f32 v46, v46, s34, 1.0
	v_exp_f32_e32 v67, v47
	v_fmaak_f32 v42, v42, v121, 0xc1e6d4ca
	v_fmaak_f32 v43, v43, v122, 0xc1e6d4ca
	v_fma_f32 v47, v47, s34, 1.0
	v_mul_f32_e32 v44, v64, v44
	v_mul_f32_e32 v45, v65, v45
	v_cvt_pk_bf16_f32 v68, v64, v65
	v_mul_f32_e32 v46, v66, v46
	v_mul_f32_e32 v47, v67, v47
	v_cvt_pk_bf16_f32 v69, v66, v67
	ds_write_b64 v120, v[68:69] offset:10272
	v_cvt_pk_bf16_f32 v80, v44, v45
	v_cvt_pk_bf16_f32 v81, v46, v47
	v_exp_f32_e32 v64, v40
	v_mul_f32_e32 v118, v114, v112
	v_mul_f32_e32 v119, v115, v112
	v_fma_f32 v40, v40, s34, 1.0
	v_exp_f32_e32 v65, v41
	v_mul_f32_e32 v121, v116, v112
	v_mul_f32_e32 v122, v117, v112
	v_fma_f32 v41, v41, s34, 1.0
	v_exp_f32_e32 v66, v42
	v_fmaak_f32 v36, v36, v118, 0xc1e6d4ca
	v_fmaak_f32 v37, v37, v119, 0xc1e6d4ca
	v_fma_f32 v42, v42, s34, 1.0
	v_exp_f32_e32 v67, v43
	v_fmaak_f32 v38, v38, v121, 0xc1e6d4ca
	v_fmaak_f32 v39, v39, v122, 0xc1e6d4ca
	v_fma_f32 v43, v43, s34, 1.0
	v_mul_f32_e32 v40, v64, v40
	v_mul_f32_e32 v41, v65, v41
	v_cvt_pk_bf16_f32 v68, v64, v65
	v_mul_f32_e32 v42, v66, v42
	v_mul_f32_e32 v43, v67, v43
	v_cvt_pk_bf16_f32 v69, v66, v67
	ds_write_b64 v120, v[68:69] offset:12448
	v_cvt_pk_bf16_f32 v82, v40, v41
	v_cvt_pk_bf16_f32 v83, v42, v43
	v_exp_f32_e32 v64, v36
	v_mul_f32_e32 v118, v114, v113
	v_mul_f32_e32 v119, v115, v113
	v_fma_f32 v36, v36, s34, 1.0
	v_exp_f32_e32 v65, v37
	v_mul_f32_e32 v121, v116, v113
	v_mul_f32_e32 v122, v117, v113
	v_fma_f32 v37, v37, s34, 1.0
	ds_read_b128 v[114:117], v71 offset:8960
	v_exp_f32_e32 v66, v38
	v_fmaak_f32 v32, v32, v118, 0xc1e6d4ca
	v_fmaak_f32 v33, v33, v119, 0xc1e6d4ca
	v_fma_f32 v38, v38, s34, 1.0
	v_exp_f32_e32 v67, v39
	v_fmaak_f32 v34, v34, v121, 0xc1e6d4ca
	v_fmaak_f32 v35, v35, v122, 0xc1e6d4ca
	v_fma_f32 v39, v39, s34, 1.0
	v_mul_f32_e32 v36, v64, v36
	v_mul_f32_e32 v37, v65, v37
	v_cvt_pk_bf16_f32 v68, v64, v65
	v_mul_f32_e32 v38, v66, v38
	v_mul_f32_e32 v39, v67, v39
	v_cvt_pk_bf16_f32 v69, v66, v67
	ds_write_b64 v120, v[68:69] offset:14624
	v_cvt_pk_bf16_f32 v84, v36, v37
	v_cvt_pk_bf16_f32 v85, v38, v39
	s_waitcnt lgkmcnt(0)
	v_exp_f32_e32 v64, v32
	v_mul_f32_e32 v118, v114, v108
	v_mul_f32_e32 v119, v115, v108
	v_fma_f32 v32, v32, s34, 1.0
	v_exp_f32_e32 v65, v33
	v_mul_f32_e32 v121, v116, v108
	v_mul_f32_e32 v122, v117, v108
	v_fma_f32 v33, v33, s34, 1.0
	v_exp_f32_e32 v66, v34
	v_fmaak_f32 v28, v28, v118, 0xc1e6d4ca
	v_fmaak_f32 v29, v29, v119, 0xc1e6d4ca
	v_fma_f32 v34, v34, s34, 1.0
	v_exp_f32_e32 v67, v35
	v_fmaak_f32 v30, v30, v121, 0xc1e6d4ca
	v_fmaak_f32 v31, v31, v122, 0xc1e6d4ca
	v_fma_f32 v35, v35, s34, 1.0
	v_mul_f32_e32 v32, v64, v32
	v_mul_f32_e32 v33, v65, v33
	v_cvt_pk_bf16_f32 v68, v64, v65
	v_mul_f32_e32 v34, v66, v34
	v_mul_f32_e32 v35, v67, v35
	v_cvt_pk_bf16_f32 v69, v66, v67
	ds_write_b64 v120, v[68:69] offset:16800
	v_cvt_pk_bf16_f32 v86, v32, v33
	v_cvt_pk_bf16_f32 v87, v34, v35
	v_exp_f32_e32 v64, v28
	v_mul_f32_e32 v118, v114, v111
	v_mul_f32_e32 v119, v115, v111
	v_fma_f32 v28, v28, s34, 1.0
	v_exp_f32_e32 v65, v29
	v_mul_f32_e32 v121, v116, v111
	v_mul_f32_e32 v122, v117, v111
	v_fma_f32 v29, v29, s34, 1.0
	v_exp_f32_e32 v66, v30
	v_fmaak_f32 v24, v24, v118, 0xc1e6d4ca
	v_fmaak_f32 v25, v25, v119, 0xc1e6d4ca
	v_fma_f32 v30, v30, s34, 1.0
	v_exp_f32_e32 v67, v31
	v_fmaak_f32 v26, v26, v121, 0xc1e6d4ca
	v_fmaak_f32 v27, v27, v122, 0xc1e6d4ca
	v_fma_f32 v31, v31, s34, 1.0
	v_mul_f32_e32 v28, v64, v28
	v_mul_f32_e32 v29, v65, v29
	v_cvt_pk_bf16_f32 v68, v64, v65
	v_mul_f32_e32 v30, v66, v30
	v_mul_f32_e32 v31, v67, v31
	v_cvt_pk_bf16_f32 v69, v66, v67
	ds_write_b64 v120, v[68:69] offset:10304
	v_cvt_pk_bf16_f32 v88, v28, v29
	v_cvt_pk_bf16_f32 v89, v30, v31
	v_exp_f32_e32 v64, v24
	v_mul_f32_e32 v118, v114, v112
	v_mul_f32_e32 v119, v115, v112
	v_fma_f32 v24, v24, s34, 1.0
	v_exp_f32_e32 v65, v25
	v_mul_f32_e32 v121, v116, v112
	v_mul_f32_e32 v122, v117, v112
	v_fma_f32 v25, v25, s34, 1.0
	v_exp_f32_e32 v66, v26
	v_fmaak_f32 v20, v20, v118, 0xc1e6d4ca
	v_fmaak_f32 v21, v21, v119, 0xc1e6d4ca
	v_fma_f32 v26, v26, s34, 1.0
	v_exp_f32_e32 v67, v27
	v_fmaak_f32 v22, v22, v121, 0xc1e6d4ca
	v_fmaak_f32 v23, v23, v122, 0xc1e6d4ca
	v_fma_f32 v27, v27, s34, 1.0
	v_mul_f32_e32 v24, v64, v24
	v_mul_f32_e32 v25, v65, v25
	v_cvt_pk_bf16_f32 v68, v64, v65
	v_mul_f32_e32 v26, v66, v26
	v_mul_f32_e32 v27, v67, v27
	v_cvt_pk_bf16_f32 v69, v66, v67
	ds_write_b64 v120, v[68:69] offset:12480
	v_cvt_pk_bf16_f32 v90, v24, v25
	v_cvt_pk_bf16_f32 v91, v26, v27
	v_exp_f32_e32 v64, v20
	v_mul_f32_e32 v118, v114, v113
	v_mul_f32_e32 v119, v115, v113
	v_fma_f32 v20, v20, s34, 1.0
	v_exp_f32_e32 v65, v21
	v_mul_f32_e32 v121, v116, v113
	v_mul_f32_e32 v122, v117, v113
	v_fma_f32 v21, v21, s34, 1.0
	ds_read_b128 v[114:117], v71 offset:9024
	v_exp_f32_e32 v66, v22
	v_fmaak_f32 v16, v16, v118, 0xc1e6d4ca
	v_fmaak_f32 v17, v17, v119, 0xc1e6d4ca
	v_fma_f32 v22, v22, s34, 1.0
	v_exp_f32_e32 v67, v23
	v_fmaak_f32 v18, v18, v121, 0xc1e6d4ca
	v_fmaak_f32 v19, v19, v122, 0xc1e6d4ca
	v_fma_f32 v23, v23, s34, 1.0
	v_mul_f32_e32 v20, v64, v20
	v_mul_f32_e32 v21, v65, v21
	v_cvt_pk_bf16_f32 v68, v64, v65
	v_mul_f32_e32 v22, v66, v22
	v_mul_f32_e32 v23, v67, v23
	v_cvt_pk_bf16_f32 v69, v66, v67
	ds_write_b64 v120, v[68:69] offset:14656
	v_cvt_pk_bf16_f32 v92, v20, v21
	v_cvt_pk_bf16_f32 v93, v22, v23
	s_waitcnt lgkmcnt(0)
	v_exp_f32_e32 v64, v16
	v_mul_f32_e32 v118, v114, v108
	v_mul_f32_e32 v119, v115, v108
	v_fma_f32 v16, v16, s34, 1.0
	v_exp_f32_e32 v65, v17
	v_mul_f32_e32 v121, v116, v108
	v_mul_f32_e32 v122, v117, v108
	v_fma_f32 v17, v17, s34, 1.0
	v_exp_f32_e32 v66, v18
	v_fmaak_f32 v12, v12, v118, 0xc1e6d4ca
	v_fmaak_f32 v13, v13, v119, 0xc1e6d4ca
	v_fma_f32 v18, v18, s34, 1.0
	v_exp_f32_e32 v67, v19
	v_fmaak_f32 v14, v14, v121, 0xc1e6d4ca
	v_fmaak_f32 v15, v15, v122, 0xc1e6d4ca
	v_fma_f32 v19, v19, s34, 1.0
	v_mul_f32_e32 v16, v64, v16
	v_mul_f32_e32 v17, v65, v17
	v_cvt_pk_bf16_f32 v68, v64, v65
	v_mul_f32_e32 v18, v66, v18
	v_mul_f32_e32 v19, v67, v19
	v_cvt_pk_bf16_f32 v69, v66, v67
	ds_write_b64 v120, v[68:69] offset:16832
	v_cvt_pk_bf16_f32 v94, v16, v17
	v_cvt_pk_bf16_f32 v95, v18, v19
	v_exp_f32_e32 v64, v12
	v_mul_f32_e32 v118, v114, v111
	v_mul_f32_e32 v119, v115, v111
	v_fma_f32 v12, v12, s34, 1.0
	v_exp_f32_e32 v65, v13
	v_mul_f32_e32 v121, v116, v111
	v_mul_f32_e32 v122, v117, v111
	v_fma_f32 v13, v13, s34, 1.0
	v_exp_f32_e32 v66, v14
	v_fmaak_f32 v8, v8, v118, 0xc1e6d4ca
	v_fmaak_f32 v9, v9, v119, 0xc1e6d4ca
	v_fma_f32 v14, v14, s34, 1.0
	v_exp_f32_e32 v67, v15
	v_fmaak_f32 v10, v10, v121, 0xc1e6d4ca
	v_fmaak_f32 v11, v11, v122, 0xc1e6d4ca
	v_fma_f32 v15, v15, s34, 1.0
	v_mul_f32_e32 v12, v64, v12
	v_mul_f32_e32 v13, v65, v13
	v_cvt_pk_bf16_f32 v68, v64, v65
	v_mul_f32_e32 v14, v66, v14
	v_mul_f32_e32 v15, v67, v15
	v_cvt_pk_bf16_f32 v69, v66, v67
	ds_write_b64 v120, v[68:69] offset:10336
	v_cvt_pk_bf16_f32 v96, v12, v13
	v_cvt_pk_bf16_f32 v97, v14, v15
	v_exp_f32_e32 v64, v8
	v_mul_f32_e32 v118, v114, v112
	v_mul_f32_e32 v119, v115, v112
	v_fma_f32 v8, v8, s34, 1.0
	v_exp_f32_e32 v65, v9
	v_mul_f32_e32 v121, v116, v112
	v_mul_f32_e32 v122, v117, v112
	v_fma_f32 v9, v9, s34, 1.0
	v_exp_f32_e32 v66, v10
	v_fmaak_f32 v4, v4, v118, 0xc1e6d4ca
	v_fmaak_f32 v5, v5, v119, 0xc1e6d4ca
	v_fma_f32 v10, v10, s34, 1.0
	v_exp_f32_e32 v67, v11
	v_fmaak_f32 v6, v6, v121, 0xc1e6d4ca
	v_fmaak_f32 v7, v7, v122, 0xc1e6d4ca
	v_fma_f32 v11, v11, s34, 1.0
	v_mul_f32_e32 v8, v64, v8
	v_mul_f32_e32 v9, v65, v9
	v_cvt_pk_bf16_f32 v68, v64, v65
	v_mul_f32_e32 v10, v66, v10
	v_mul_f32_e32 v11, v67, v11
	v_cvt_pk_bf16_f32 v69, v66, v67
	ds_write_b64 v120, v[68:69] offset:12512
	v_cvt_pk_bf16_f32 v98, v8, v9
	v_cvt_pk_bf16_f32 v99, v10, v11
	v_exp_f32_e32 v64, v4
	v_mul_f32_e32 v118, v114, v113
	v_mul_f32_e32 v119, v115, v113
	v_fma_f32 v4, v4, s34, 1.0
	v_exp_f32_e32 v65, v5
	v_mul_f32_e32 v121, v116, v113
	v_mul_f32_e32 v122, v117, v113
	v_fma_f32 v5, v5, s34, 1.0
	v_exp_f32_e32 v66, v6
	v_fmaak_f32 v0, v0, v118, 0xc1e6d4ca
	v_fmaak_f32 v1, v1, v119, 0xc1e6d4ca
	v_fma_f32 v6, v6, s34, 1.0
	v_exp_f32_e32 v67, v7
	v_fmaak_f32 v2, v2, v121, 0xc1e6d4ca
	v_fmaak_f32 v3, v3, v122, 0xc1e6d4ca
	v_fma_f32 v7, v7, s34, 1.0
	v_mul_f32_e32 v4, v64, v4
	v_mul_f32_e32 v5, v65, v5
	v_cvt_pk_bf16_f32 v68, v64, v65
	v_mul_f32_e32 v6, v66, v6
	v_mul_f32_e32 v7, v67, v7
	v_cvt_pk_bf16_f32 v69, v66, v67
	ds_write_b64 v120, v[68:69] offset:14688
	v_cvt_pk_bf16_f32 v104, v4, v5
	v_cvt_pk_bf16_f32 v105, v6, v7
	v_exp_f32_e32 v64, v0
	v_fma_f32 v0, v0, s34, 1.0
	v_exp_f32_e32 v65, v1
	v_fma_f32 v1, v1, s34, 1.0
	v_exp_f32_e32 v66, v2
	v_fma_f32 v2, v2, s34, 1.0
	v_exp_f32_e32 v67, v3
	v_fma_f32 v3, v3, s34, 1.0
	v_mul_f32_e32 v0, v64, v0
	v_mul_f32_e32 v1, v65, v1
	v_cvt_pk_bf16_f32 v68, v64, v65
	v_mul_f32_e32 v2, v66, v2
	v_mul_f32_e32 v3, v67, v3
	v_cvt_pk_bf16_f32 v69, v66, v67
	ds_write_b64 v120, v[68:69] offset:16864
	v_cvt_pk_bf16_f32 v106, v0, v1
	v_cvt_pk_bf16_f32 v107, v2, v3
	s_movk_i32 s34, 0x88
	v_and_b32_e32 v64, 32, v100
	v_and_b32_e32 v66, 16, v100
	v_mad_u32_u24 v65, v101, s34, v64
	v_add_u32_e32 v65, s6, v65
	v_add_u32_e32 v67, v65, v66
	v_sub_u32_e32 v65, v65, v66
	v_lshrrev_b32_e32 v68, 1, v100
	v_and_b32_e32 v68, 16, v68
	v_bfe_u32 v69, v100, 2, 2
	v_or_b32_e32 v68, v68, v69
	v_and_b32_e32 v69, 3, v100
	v_lshlrev_b32_e32 v69, 3, v69
	v_mad_u32_u24 v68, v68, s34, v69
	v_add_u32_e32 v68, s6, v68
	s_movk_i32 s35, 0x44
	v_mul_u32_u24_e32 v66, s35, v66
	v_add_u32_e32 v69, v68, v66
	v_sub_u32_e32 v68, v68, v66
	ds_read_b64 v[0:1], v67 offset:10240
	ds_read_b64 v[2:3], v65 offset:10264
	ds_read_b64 v[4:5], v67 offset:10304
	ds_read_b64 v[6:7], v65 offset:10328
	ds_read_b64 v[8:9], v67 offset:12424
	ds_read_b64 v[10:11], v67 offset:12416
	ds_read_b64 v[12:13], v67 offset:12488
	ds_read_b64 v[14:15], v67 offset:12480
	ds_read_b64 v[16:17], v65 offset:14608
	ds_read_b64 v[18:19], v67 offset:14600
	ds_read_b64 v[20:21], v65 offset:14672
	ds_read_b64 v[22:23], v67 offset:14664
	ds_read_b64 v[24:25], v65 offset:16792
	ds_read_b64 v[26:27], v65 offset:16784
	ds_read_b64 v[28:29], v65 offset:16856
	ds_read_b64 v[30:31], v65 offset:16848
	ds_read_b64_tr_b16 v[32:33], v69 offset:10240
	ds_read_b64_tr_b16 v[34:35], v68 offset:11872
	ds_read_b64_tr_b16 v[36:37], v69 offset:14592
	ds_read_b64_tr_b16 v[38:39], v68 offset:16224
	ds_read_b64_tr_b16 v[40:41], v69 offset:10816
	ds_read_b64_tr_b16 v[42:43], v69 offset:10272
	ds_read_b64_tr_b16 v[44:45], v69 offset:15168
	ds_read_b64_tr_b16 v[46:47], v69 offset:14624
	ds_read_b64_tr_b16 v[48:49], v68 offset:11392
	ds_read_b64_tr_b16 v[50:51], v69 offset:10848
	ds_read_b64_tr_b16 v[52:53], v68 offset:15744
	ds_read_b64_tr_b16 v[54:55], v69 offset:15200
	ds_read_b64_tr_b16 v[56:57], v68 offset:11968
	ds_read_b64_tr_b16 v[58:59], v68 offset:11424
	ds_read_b64_tr_b16 v[60:61], v68 offset:16320
	ds_read_b64_tr_b16 v[62:63], v68 offset:15776
	ds_read2st64_b32 v[116:117], v102 offset0:22 offset1:23
	s_waitcnt lgkmcnt(0)
	ds_write_b64 v120, v[72:73] offset:10240
	ds_write_b64 v120, v[74:75] offset:12416
	ds_write_b64 v120, v[76:77] offset:14592
	ds_write_b64 v120, v[78:79] offset:16768
	ds_write_b64 v120, v[80:81] offset:10272
	ds_write_b64 v120, v[82:83] offset:12448
	ds_write_b64 v120, v[84:85] offset:14624
	ds_write_b64 v120, v[86:87] offset:16800
	ds_write_b64 v120, v[88:89] offset:10304
	ds_write_b64 v120, v[90:91] offset:12480
	ds_write_b64 v120, v[92:93] offset:14656
	ds_write_b64 v120, v[94:95] offset:16832
	ds_write_b64 v120, v[96:97] offset:10336
	ds_write_b64 v120, v[98:99] offset:12512
	ds_write_b64 v120, v[104:105] offset:14688
	ds_write_b64 v120, v[106:107] offset:16864
	v_and_b32_e32 v110, 1, v100
	v_cmp_eq_u32_e32 vcc, 0, v110
	v_mov_b32_e32 v110, 0xeeeeeeee
	v_mov_b32_e32 v111, 0x44444444
	s_mov_b32 s32, 0x2b8cbccc
	s_mov_b32 s33, 0
	v_cndmask_b32_e32 v64, v110, v111, vcc
	v_mov_b32_e32 v68, 0x3f803f80
	v_mov_b32_e32 v69, v68
	v_mov_b32_e32 v70, v68
	v_mov_b32_e32 v71, v68
	v_mov_b64_e32 v[72:73], s[32:33]
	v_mov_b64_e32 v[76:77], s[32:33]
	v_mov_b64_e32 v[80:81], s[32:33]
	v_mov_b64_e32 v[84:85], s[32:33]
	v_mov_b64_e32 v[88:89], s[32:33]
	v_mov_b64_e32 v[92:93], s[32:33]
	v_mov_b64_e32 v[96:97], s[32:33]
	v_mov_b64_e32 v[104:105], s[32:33]
	s_movk_i32 s30, 100
	v_mov_b32_e32 v122, 0
	v_mov_b32_e32 v121, 0
	s_waitcnt lgkmcnt(0)
	v_mov_b32_dpp v112, v116 quad_perm:[0,2,0,2] row_mask:0xf bank_mask:0xf
	v_mov_b32_dpp v113, v116 quad_perm:[1,3,1,3] row_mask:0xf bank_mask:0xf
	v_mov_b32_dpp v114, v117 quad_perm:[0,2,0,2] row_mask:0xf bank_mask:0xf
	v_mov_b32_dpp v115, v117 quad_perm:[1,3,1,3] row_mask:0xf bank_mask:0xf
	v_smfmac_f32_16x16x64_bf16 v[72:75], v[68:71], v[0:7], v64
	v_smfmac_f32_16x16x64_bf16 v[76:79], v[68:71], v[8:15], v64
	v_smfmac_f32_16x16x64_bf16 v[80:83], v[68:71], v[16:23], v64
	v_smfmac_f32_16x16x64_bf16 v[84:87], v[68:71], v[24:31], v64
	s_nop 4
